# hot loop headers (8 GEMM K-loops, 2 scan recurrence loops) aligned to 256 bytes instead of 64
# baseline (speedup 1.0000x reference)
.LBB0_186:
	s_ashr_i32 s25, s24, 31
	s_lshl_b64 s[28:29], s[24:25], 20
	s_ashr_i32 s27, s26, 31
	v_lshl_add_u64 v[146:147], v[160:161], 0, s[28:29]
	s_lshl_b64 s[28:29], s[26:27], 20
	v_lshl_add_u64 v[150:151], v[128:129], 0, s[28:29]
	v_cndmask_b32_e64 v154, v0, v150, s[4:5]
	v_lshl_add_u64 v[158:159], v[0:1], 0, s[18:19]
	v_mov_b32_e32 v0, 0
	v_cndmask_b32_e64 v153, v3, v147, s[4:5]
	v_cndmask_b32_e64 v152, v2, v146, s[4:5]
	v_cndmask_b32_e64 v155, v1, v151, s[4:5]
	v_lshl_add_u64 v[156:157], v[2:3], 0, s[14:15]
	s_mov_b32 s25, -2
	v_mov_b32_e32 v1, v0
	v_mov_b32_e32 v2, v0
	v_mov_b32_e32 v3, v0
	v_mov_b32_e32 v4, v0
	v_mov_b32_e32 v5, v0
	v_mov_b32_e32 v6, v0
	v_mov_b32_e32 v7, v0
	v_mov_b32_e32 v8, v0
	v_mov_b32_e32 v9, v0
	v_mov_b32_e32 v10, v0
	v_mov_b32_e32 v11, v0
	v_mov_b32_e32 v12, v0
	v_mov_b32_e32 v13, v0
	v_mov_b32_e32 v14, v0
	v_mov_b32_e32 v15, v0
	v_mov_b32_e32 v24, v0
	v_mov_b32_e32 v25, v0
	v_mov_b32_e32 v26, v0
	v_mov_b32_e32 v27, v0
	v_mov_b32_e32 v28, v0
	v_mov_b32_e32 v29, v0
	v_mov_b32_e32 v30, v0
	v_mov_b32_e32 v31, v0
	v_mov_b32_e32 v40, v0
	v_mov_b32_e32 v41, v0
	v_mov_b32_e32 v42, v0
	v_mov_b32_e32 v43, v0
	v_mov_b32_e32 v44, v0
	v_mov_b32_e32 v45, v0
	v_mov_b32_e32 v46, v0
	v_mov_b32_e32 v47, v0
	v_mov_b32_e32 v16, v0
	v_mov_b32_e32 v17, v0
	v_mov_b32_e32 v18, v0
	v_mov_b32_e32 v19, v0
	v_mov_b32_e32 v20, v0
	v_mov_b32_e32 v21, v0
	v_mov_b32_e32 v22, v0
	v_mov_b32_e32 v23, v0
	v_mov_b32_e32 v32, v0
	v_mov_b32_e32 v33, v0
	v_mov_b32_e32 v34, v0
	v_mov_b32_e32 v35, v0
	v_mov_b32_e32 v36, v0
	v_mov_b32_e32 v37, v0
	v_mov_b32_e32 v38, v0
	v_mov_b32_e32 v39, v0
	v_mov_b32_e32 v48, v0
	v_mov_b32_e32 v49, v0
	v_mov_b32_e32 v50, v0
	v_mov_b32_e32 v51, v0
	v_mov_b32_e32 v52, v0
	v_mov_b32_e32 v53, v0
	v_mov_b32_e32 v54, v0
	v_mov_b32_e32 v55, v0
	v_mov_b32_e32 v56, v0
	v_mov_b32_e32 v57, v0
	v_mov_b32_e32 v58, v0
	v_mov_b32_e32 v59, v0
	v_mov_b32_e32 v60, v0
	v_mov_b32_e32 v61, v0
	v_mov_b32_e32 v62, v0
	v_mov_b32_e32 v63, v0
	v_mov_b32_e32 v64, v0
	v_mov_b32_e32 v65, v0
	v_mov_b32_e32 v66, v0
	v_mov_b32_e32 v67, v0
	v_mov_b32_e32 v68, v0
	v_mov_b32_e32 v69, v0
	v_mov_b32_e32 v70, v0
	v_mov_b32_e32 v71, v0
	v_mov_b32_e32 v72, v0
	v_mov_b32_e32 v73, v0
	v_mov_b32_e32 v74, v0
	v_mov_b32_e32 v75, v0
	v_mov_b32_e32 v76, v0
	v_mov_b32_e32 v77, v0
	v_mov_b32_e32 v78, v0
	v_mov_b32_e32 v79, v0
	v_mov_b32_e32 v88, v0
	v_mov_b32_e32 v89, v0
	v_mov_b32_e32 v90, v0
	v_mov_b32_e32 v91, v0
	v_mov_b32_e32 v92, v0
	v_mov_b32_e32 v93, v0
	v_mov_b32_e32 v94, v0
	v_mov_b32_e32 v95, v0
	v_mov_b32_e32 v104, v0
	v_mov_b32_e32 v105, v0
	v_mov_b32_e32 v106, v0
	v_mov_b32_e32 v107, v0
	v_mov_b32_e32 v108, v0
	v_mov_b32_e32 v109, v0
	v_mov_b32_e32 v110, v0
	v_mov_b32_e32 v111, v0
	v_mov_b32_e32 v80, v0
	v_mov_b32_e32 v81, v0
	v_mov_b32_e32 v82, v0
	v_mov_b32_e32 v83, v0
	v_mov_b32_e32 v84, v0
	v_mov_b32_e32 v85, v0
	v_mov_b32_e32 v86, v0
	v_mov_b32_e32 v87, v0
	v_mov_b32_e32 v96, v0
	v_mov_b32_e32 v97, v0
	v_mov_b32_e32 v98, v0
	v_mov_b32_e32 v99, v0
	v_mov_b32_e32 v100, v0
	v_mov_b32_e32 v101, v0
	v_mov_b32_e32 v102, v0
	v_mov_b32_e32 v103, v0
	v_mov_b32_e32 v112, v0
	v_mov_b32_e32 v113, v0
	v_mov_b32_e32 v114, v0
	v_mov_b32_e32 v115, v0
	v_mov_b32_e32 v116, v0
	v_mov_b32_e32 v117, v0
	v_mov_b32_e32 v118, v0
	v_mov_b32_e32 v119, v0
	v_mov_b32_e32 v120, v0
	v_mov_b32_e32 v121, v0
	v_mov_b32_e32 v122, v0
	v_mov_b32_e32 v123, v0
	v_mov_b32_e32 v124, v0
	v_mov_b32_e32 v125, v0
	v_mov_b32_e32 v126, v0
	v_mov_b32_e32 v127, v0
	.p2align	8

.LBB0_722:
	s_andn2_b64 vcc, exec, s[14:15]
	s_cbranch_vccz .LBB0_725
	.p2align	8

.LBB0_899:
	s_ashr_i32 s29, s28, 31
	s_lshl_b64 s[36:37], s[28:29], 20
	s_ashr_i32 s27, s26, 31
	v_lshl_add_u64 v[146:147], v[128:129], 0, s[36:37]
	s_lshl_b64 s[36:37], s[26:27], 20
	v_lshl_add_u64 v[150:151], v[130:131], 0, s[36:37]
	v_lshl_add_u64 v[152:153], v[156:157], 0, s[22:23]
	v_cndmask_b32_e64 v155, v145, v147, s[6:7]
	v_cndmask_b32_e64 v154, v144, v146, s[6:7]
	v_cndmask_b32_e64 v157, v157, v151, s[6:7]
	v_cndmask_b32_e64 v156, v156, v150, s[6:7]
	v_lshl_add_u64 v[158:159], v[144:145], 0, v[136:137]
	v_lshl_add_u64 v[166:167], v[144:145], 0, v[138:139]
	s_mov_b32 s27, -2
	s_mov_b64 s[36:37], 0
	.p2align	8

.LBB0_995:
	s_ashr_i32 s27, s26, 31
	s_lshl_b64 s[6:7], s[26:27], 20
	s_ashr_i32 s25, s24, 31
	v_lshl_add_u64 v[4:5], v[160:161], 0, s[6:7]
	s_lshl_b64 s[6:7], s[24:25], 20
	v_lshl_add_u64 v[6:7], v[128:129], 0, s[6:7]
	s_ashr_i32 s23, s22, 31
	v_cndmask_b32_e64 v7, v1, v7, s[4:5]
	v_cndmask_b32_e64 v6, v0, v6, s[4:5]
	s_lshl_b64 s[6:7], s[22:23], 7
	v_cndmask_b32_e64 v5, v3, v5, s[4:5]
	v_cndmask_b32_e64 v4, v2, v4, s[4:5]
	v_lshl_add_u64 v[156:157], v[6:7], 0, s[6:7]
	v_lshl_add_u64 v[154:155], v[4:5], 0, s[6:7]
	v_cndmask_b32_e64 v158, v0, v156, s[4:5]
	v_lshl_add_u64 v[170:171], v[0:1], 0, s[20:21]
	v_mov_b32_e32 v0, 0
	v_cndmask_b32_e64 v159, v3, v155, s[4:5]
	v_cndmask_b32_e64 v138, v2, v154, s[4:5]
	v_cndmask_b32_e64 v167, v1, v157, s[4:5]
	s_add_i32 s6, s40, -2
	v_lshl_add_u64 v[168:169], v[2:3], 0, s[16:17]
	s_mov_b32 s7, 0
	v_mov_b32_e32 v1, v0
	v_mov_b32_e32 v2, v0
	v_mov_b32_e32 v3, v0
	v_mov_b32_e32 v8, v0
	v_mov_b32_e32 v9, v0
	v_mov_b32_e32 v10, v0
	v_mov_b32_e32 v11, v0
	v_mov_b32_e32 v16, v0
	v_mov_b32_e32 v17, v0
	v_mov_b32_e32 v18, v0
	v_mov_b32_e32 v19, v0
	v_mov_b32_e32 v24, v0
	v_mov_b32_e32 v25, v0
	v_mov_b32_e32 v26, v0
	v_mov_b32_e32 v27, v0
	v_mov_b32_e32 v32, v0
	v_mov_b32_e32 v33, v0
	v_mov_b32_e32 v34, v0
	v_mov_b32_e32 v35, v0
	v_mov_b32_e32 v40, v0
	v_mov_b32_e32 v41, v0
	v_mov_b32_e32 v42, v0
	v_mov_b32_e32 v43, v0
	v_mov_b32_e32 v48, v0
	v_mov_b32_e32 v49, v0
	v_mov_b32_e32 v50, v0
	v_mov_b32_e32 v51, v0
	v_mov_b32_e32 v56, v0
	v_mov_b32_e32 v57, v0
	v_mov_b32_e32 v58, v0
	v_mov_b32_e32 v59, v0
	v_mov_b32_e32 v4, v0
	v_mov_b32_e32 v5, v0
	v_mov_b32_e32 v6, v0
	v_mov_b32_e32 v7, v0
	v_mov_b32_e32 v12, v0
	v_mov_b32_e32 v13, v0
	v_mov_b32_e32 v14, v0
	v_mov_b32_e32 v15, v0
	v_mov_b32_e32 v20, v0
	v_mov_b32_e32 v21, v0
	v_mov_b32_e32 v22, v0
	v_mov_b32_e32 v23, v0
	v_mov_b32_e32 v28, v0
	v_mov_b32_e32 v29, v0
	v_mov_b32_e32 v30, v0
	v_mov_b32_e32 v31, v0
	v_mov_b32_e32 v36, v0
	v_mov_b32_e32 v37, v0
	v_mov_b32_e32 v38, v0
	v_mov_b32_e32 v39, v0
	v_mov_b32_e32 v44, v0
	v_mov_b32_e32 v45, v0
	v_mov_b32_e32 v46, v0
	v_mov_b32_e32 v47, v0
	v_mov_b32_e32 v52, v0
	v_mov_b32_e32 v53, v0
	v_mov_b32_e32 v54, v0
	v_mov_b32_e32 v55, v0
	v_mov_b32_e32 v60, v0
	v_mov_b32_e32 v61, v0
	v_mov_b32_e32 v62, v0
	v_mov_b32_e32 v63, v0
	v_mov_b32_e32 v64, v0
	v_mov_b32_e32 v65, v0
	v_mov_b32_e32 v66, v0
	v_mov_b32_e32 v67, v0
	v_mov_b32_e32 v72, v0
	v_mov_b32_e32 v73, v0
	v_mov_b32_e32 v74, v0
	v_mov_b32_e32 v75, v0
	v_mov_b32_e32 v80, v0
	v_mov_b32_e32 v81, v0
	v_mov_b32_e32 v82, v0
	v_mov_b32_e32 v83, v0
	v_mov_b32_e32 v88, v0
	v_mov_b32_e32 v89, v0
	v_mov_b32_e32 v90, v0
	v_mov_b32_e32 v91, v0
	v_mov_b32_e32 v96, v0
	v_mov_b32_e32 v97, v0
	v_mov_b32_e32 v98, v0
	v_mov_b32_e32 v99, v0
	v_mov_b32_e32 v104, v0
	v_mov_b32_e32 v105, v0
	v_mov_b32_e32 v106, v0
	v_mov_b32_e32 v107, v0
	v_mov_b32_e32 v112, v0
	v_mov_b32_e32 v113, v0
	v_mov_b32_e32 v114, v0
	v_mov_b32_e32 v115, v0
	v_mov_b32_e32 v120, v0
	v_mov_b32_e32 v121, v0
	v_mov_b32_e32 v122, v0
	v_mov_b32_e32 v123, v0
	v_mov_b32_e32 v68, v0
	v_mov_b32_e32 v69, v0
	v_mov_b32_e32 v70, v0
	v_mov_b32_e32 v71, v0
	v_mov_b32_e32 v76, v0
	v_mov_b32_e32 v77, v0
	v_mov_b32_e32 v78, v0
	v_mov_b32_e32 v79, v0
	v_mov_b32_e32 v84, v0
	v_mov_b32_e32 v85, v0
	v_mov_b32_e32 v86, v0
	v_mov_b32_e32 v87, v0
	v_mov_b32_e32 v92, v0
	v_mov_b32_e32 v93, v0
	v_mov_b32_e32 v94, v0
	v_mov_b32_e32 v95, v0
	v_mov_b32_e32 v100, v0
	v_mov_b32_e32 v101, v0
	v_mov_b32_e32 v102, v0
	v_mov_b32_e32 v103, v0
	v_mov_b32_e32 v108, v0
	v_mov_b32_e32 v109, v0
	v_mov_b32_e32 v110, v0
	v_mov_b32_e32 v111, v0
	v_mov_b32_e32 v116, v0
	v_mov_b32_e32 v117, v0
	v_mov_b32_e32 v118, v0
	v_mov_b32_e32 v119, v0
	v_mov_b32_e32 v124, v0
	v_mov_b32_e32 v125, v0
	v_mov_b32_e32 v126, v0
	v_mov_b32_e32 v127, v0
	.p2align	8

.LBB0_1134:
	v_lshl_add_u64 v[150:151], v[150:151], 0, s[24:25]
	v_lshl_add_u64 v[152:153], v[142:143], 0, v[134:135]
	v_lshl_add_u64 v[154:155], v[142:143], 0, v[136:137]
	s_mov_b32 s29, -2
	s_mov_b64 s[10:11], 0
	.p2align	8

.LBB0_1230:
	s_ashr_i32 s23, s22, 31
	s_lshl_b64 s[24:25], s[22:23], 20
	s_add_u32 s0, s11, s24
	s_addc_u32 s1, s65, s25
	s_and_b64 s[24:25], s[4:5], exec
	s_cselect_b32 s1, s1, s29
	s_cselect_b32 s0, s0, s28
	s_ashr_i32 s21, s20, 31
	s_lshl_b64 s[24:25], s[20:21], 20
	s_add_u32 s19, s80, s24
	s_addc_u32 s21, s81, s25
	s_and_b64 s[24:25], s[4:5], exec
	s_cselect_b32 s21, s21, s31
	s_cselect_b32 s23, s19, s30
	s_ashr_i32 s19, s18, 31
	s_lshl_b64 s[26:27], s[18:19], 7
	s_add_u32 s24, s0, s26
	s_addc_u32 s25, s1, s27
	s_add_u32 s26, s23, s26
	s_addc_u32 s27, s21, s27
	s_and_b64 s[36:37], s[4:5], exec
	s_cselect_b32 s19, s25, s29
	s_cselect_b32 s21, s24, s28
	s_cselect_b32 s23, s27, s31
	s_cselect_b32 s39, s26, s30
	s_add_i32 s40, s38, -2
	s_add_u32 s28, s28, 0x80080
	s_addc_u32 s29, s29, 0
	s_add_u32 s41, s30, 0x100
	v_mov_b32_e32 v0, 0
	s_addc_u32 s42, s31, 0
	s_mov_b32 s30, 0
	v_mov_b32_e32 v1, v0
	v_mov_b32_e32 v2, v0
	v_mov_b32_e32 v3, v0
	v_mov_b32_e32 v4, v0
	v_mov_b32_e32 v5, v0
	v_mov_b32_e32 v6, v0
	v_mov_b32_e32 v7, v0
	v_mov_b32_e32 v8, v0
	v_mov_b32_e32 v9, v0
	v_mov_b32_e32 v10, v0
	v_mov_b32_e32 v11, v0
	v_mov_b32_e32 v16, v0
	v_mov_b32_e32 v17, v0
	v_mov_b32_e32 v18, v0
	v_mov_b32_e32 v19, v0
	v_mov_b32_e32 v24, v0
	v_mov_b32_e32 v25, v0
	v_mov_b32_e32 v26, v0
	v_mov_b32_e32 v27, v0
	v_mov_b32_e32 v32, v0
	v_mov_b32_e32 v33, v0
	v_mov_b32_e32 v34, v0
	v_mov_b32_e32 v35, v0
	v_mov_b32_e32 v40, v0
	v_mov_b32_e32 v41, v0
	v_mov_b32_e32 v42, v0
	v_mov_b32_e32 v43, v0
	v_mov_b32_e32 v48, v0
	v_mov_b32_e32 v49, v0
	v_mov_b32_e32 v50, v0
	v_mov_b32_e32 v51, v0
	v_mov_b32_e32 v12, v0
	v_mov_b32_e32 v13, v0
	v_mov_b32_e32 v14, v0
	v_mov_b32_e32 v15, v0
	v_mov_b32_e32 v20, v0
	v_mov_b32_e32 v21, v0
	v_mov_b32_e32 v22, v0
	v_mov_b32_e32 v23, v0
	v_mov_b32_e32 v28, v0
	v_mov_b32_e32 v29, v0
	v_mov_b32_e32 v30, v0
	v_mov_b32_e32 v31, v0
	v_mov_b32_e32 v36, v0
	v_mov_b32_e32 v37, v0
	v_mov_b32_e32 v38, v0
	v_mov_b32_e32 v39, v0
	v_mov_b32_e32 v44, v0
	v_mov_b32_e32 v45, v0
	v_mov_b32_e32 v46, v0
	v_mov_b32_e32 v47, v0
	v_mov_b32_e32 v52, v0
	v_mov_b32_e32 v53, v0
	v_mov_b32_e32 v54, v0
	v_mov_b32_e32 v55, v0
	v_mov_b32_e32 v56, v0
	v_mov_b32_e32 v57, v0
	v_mov_b32_e32 v58, v0
	v_mov_b32_e32 v59, v0
	v_mov_b32_e32 v60, v0
	v_mov_b32_e32 v61, v0
	v_mov_b32_e32 v62, v0
	v_mov_b32_e32 v63, v0
	v_mov_b32_e32 v64, v0
	v_mov_b32_e32 v65, v0
	v_mov_b32_e32 v66, v0
	v_mov_b32_e32 v67, v0
	v_mov_b32_e32 v68, v0
	v_mov_b32_e32 v69, v0
	v_mov_b32_e32 v70, v0
	v_mov_b32_e32 v71, v0
	v_mov_b32_e32 v72, v0
	v_mov_b32_e32 v73, v0
	v_mov_b32_e32 v74, v0
	v_mov_b32_e32 v75, v0
	v_mov_b32_e32 v80, v0
	v_mov_b32_e32 v81, v0
	v_mov_b32_e32 v82, v0
	v_mov_b32_e32 v83, v0
	v_mov_b32_e32 v88, v0
	v_mov_b32_e32 v89, v0
	v_mov_b32_e32 v90, v0
	v_mov_b32_e32 v91, v0
	v_mov_b32_e32 v96, v0
	v_mov_b32_e32 v97, v0
	v_mov_b32_e32 v98, v0
	v_mov_b32_e32 v99, v0
	v_mov_b32_e32 v104, v0
	v_mov_b32_e32 v105, v0
	v_mov_b32_e32 v106, v0
	v_mov_b32_e32 v107, v0
	v_mov_b32_e32 v112, v0
	v_mov_b32_e32 v113, v0
	v_mov_b32_e32 v114, v0
	v_mov_b32_e32 v115, v0
	v_mov_b32_e32 v76, v0
	v_mov_b32_e32 v77, v0
	v_mov_b32_e32 v78, v0
	v_mov_b32_e32 v79, v0
	v_mov_b32_e32 v84, v0
	v_mov_b32_e32 v85, v0
	v_mov_b32_e32 v86, v0
	v_mov_b32_e32 v87, v0
	v_mov_b32_e32 v92, v0
	v_mov_b32_e32 v93, v0
	v_mov_b32_e32 v94, v0
	v_mov_b32_e32 v95, v0
	v_mov_b32_e32 v100, v0
	v_mov_b32_e32 v101, v0
	v_mov_b32_e32 v102, v0
	v_mov_b32_e32 v103, v0
	v_mov_b32_e32 v108, v0
	v_mov_b32_e32 v109, v0
	v_mov_b32_e32 v110, v0
	v_mov_b32_e32 v111, v0
	v_mov_b32_e32 v116, v0
	v_mov_b32_e32 v117, v0
	v_mov_b32_e32 v118, v0
	v_mov_b32_e32 v119, v0
	v_mov_b32_e32 v120, v0
	v_mov_b32_e32 v121, v0
	v_mov_b32_e32 v122, v0
	v_mov_b32_e32 v123, v0
	v_mov_b32_e32 v124, v0
	v_mov_b32_e32 v125, v0
	v_mov_b32_e32 v126, v0
	v_mov_b32_e32 v127, v0
	.p2align	8

.LBB0_1816:
	s_andn2_b64 vcc, exec, s[4:5]
	s_cbranch_vccz .LBB0_1819
	.p2align	8

.LBB0_1993:
	s_ashr_i32 s25, s24, 31
	s_lshl_b64 s[0:1], s[24:25], 20
	s_add_u32 s28, s35, s0
	s_addc_u32 s29, s44, s1
	s_and_b64 s[0:1], s[4:5], exec
	s_cselect_b32 s25, s29, s39
	s_cselect_b32 s65, s28, s38
	s_ashr_i32 s27, s26, 31
	s_lshl_b64 s[0:1], s[26:27], 20
	s_add_u32 s30, s45, s0
	s_addc_u32 s31, s46, s1
	s_and_b64 s[0:1], s[4:5], exec
	s_cselect_b32 s27, s31, s41
	s_cselect_b32 s66, s30, s40
	s_add_u32 s38, s38, 0x80080
	s_addc_u32 s39, s39, 0
	s_add_u32 s67, s40, 0x100
	v_mov_b32_e32 v0, 0
	s_addc_u32 s68, s41, 0
	s_mov_b32 s69, -2
	v_mov_b32_e32 v1, v0
	v_mov_b32_e32 v2, v0
	v_mov_b32_e32 v3, v0
	v_mov_b32_e32 v4, v0
	v_mov_b32_e32 v5, v0
	v_mov_b32_e32 v6, v0
	v_mov_b32_e32 v7, v0
	v_mov_b32_e32 v8, v0
	v_mov_b32_e32 v9, v0
	v_mov_b32_e32 v10, v0
	v_mov_b32_e32 v11, v0
	v_mov_b32_e32 v20, v0
	v_mov_b32_e32 v21, v0
	v_mov_b32_e32 v22, v0
	v_mov_b32_e32 v23, v0
	v_mov_b32_e32 v24, v0
	v_mov_b32_e32 v25, v0
	v_mov_b32_e32 v26, v0
	v_mov_b32_e32 v27, v0
	v_mov_b32_e32 v36, v0
	v_mov_b32_e32 v37, v0
	v_mov_b32_e32 v38, v0
	v_mov_b32_e32 v39, v0
	v_mov_b32_e32 v40, v0
	v_mov_b32_e32 v41, v0
	v_mov_b32_e32 v42, v0
	v_mov_b32_e32 v43, v0
	v_mov_b32_e32 v52, v0
	v_mov_b32_e32 v53, v0
	v_mov_b32_e32 v54, v0
	v_mov_b32_e32 v55, v0
	v_mov_b32_e32 v12, v0
	v_mov_b32_e32 v13, v0
	v_mov_b32_e32 v14, v0
	v_mov_b32_e32 v15, v0
	v_mov_b32_e32 v16, v0
	v_mov_b32_e32 v17, v0
	v_mov_b32_e32 v18, v0
	v_mov_b32_e32 v19, v0
	v_mov_b32_e32 v28, v0
	v_mov_b32_e32 v29, v0
	v_mov_b32_e32 v30, v0
	v_mov_b32_e32 v31, v0
	v_mov_b32_e32 v32, v0
	v_mov_b32_e32 v33, v0
	v_mov_b32_e32 v34, v0
	v_mov_b32_e32 v35, v0
	v_mov_b32_e32 v44, v0
	v_mov_b32_e32 v45, v0
	v_mov_b32_e32 v46, v0
	v_mov_b32_e32 v47, v0
	v_mov_b32_e32 v48, v0
	v_mov_b32_e32 v49, v0
	v_mov_b32_e32 v50, v0
	v_mov_b32_e32 v51, v0
	v_mov_b32_e32 v56, v0
	v_mov_b32_e32 v57, v0
	v_mov_b32_e32 v58, v0
	v_mov_b32_e32 v59, v0
	v_mov_b32_e32 v60, v0
	v_mov_b32_e32 v61, v0
	v_mov_b32_e32 v62, v0
	v_mov_b32_e32 v63, v0
	v_mov_b32_e32 v64, v0
	v_mov_b32_e32 v65, v0
	v_mov_b32_e32 v66, v0
	v_mov_b32_e32 v67, v0
	v_mov_b32_e32 v68, v0
	v_mov_b32_e32 v69, v0
	v_mov_b32_e32 v70, v0
	v_mov_b32_e32 v71, v0
	v_mov_b32_e32 v72, v0
	v_mov_b32_e32 v73, v0
	v_mov_b32_e32 v74, v0
	v_mov_b32_e32 v75, v0
	v_mov_b32_e32 v84, v0
	v_mov_b32_e32 v85, v0
	v_mov_b32_e32 v86, v0
	v_mov_b32_e32 v87, v0
	v_mov_b32_e32 v88, v0
	v_mov_b32_e32 v89, v0
	v_mov_b32_e32 v90, v0
	v_mov_b32_e32 v91, v0
	v_mov_b32_e32 v100, v0
	v_mov_b32_e32 v101, v0
	v_mov_b32_e32 v102, v0
	v_mov_b32_e32 v103, v0
	v_mov_b32_e32 v104, v0
	v_mov_b32_e32 v105, v0
	v_mov_b32_e32 v106, v0
	v_mov_b32_e32 v107, v0
	v_mov_b32_e32 v116, v0
	v_mov_b32_e32 v117, v0
	v_mov_b32_e32 v118, v0
	v_mov_b32_e32 v119, v0
	v_mov_b32_e32 v76, v0
	v_mov_b32_e32 v77, v0
	v_mov_b32_e32 v78, v0
	v_mov_b32_e32 v79, v0
	v_mov_b32_e32 v80, v0
	v_mov_b32_e32 v81, v0
	v_mov_b32_e32 v82, v0
	v_mov_b32_e32 v83, v0
	v_mov_b32_e32 v92, v0
	v_mov_b32_e32 v93, v0
	v_mov_b32_e32 v94, v0
	v_mov_b32_e32 v95, v0
	v_mov_b32_e32 v96, v0
	v_mov_b32_e32 v97, v0
	v_mov_b32_e32 v98, v0
	v_mov_b32_e32 v99, v0
	v_mov_b32_e32 v108, v0
	v_mov_b32_e32 v109, v0
	v_mov_b32_e32 v110, v0
	v_mov_b32_e32 v111, v0
	v_mov_b32_e32 v112, v0
	v_mov_b32_e32 v113, v0
	v_mov_b32_e32 v114, v0
	v_mov_b32_e32 v115, v0
	v_mov_b32_e32 v120, v0
	v_mov_b32_e32 v121, v0
	v_mov_b32_e32 v122, v0
	v_mov_b32_e32 v123, v0
	v_mov_b32_e32 v124, v0
	v_mov_b32_e32 v125, v0
	v_mov_b32_e32 v126, v0
	v_mov_b32_e32 v127, v0
	.p2align	8

.LBB0_2153:
	s_ashr_i32 s19, s18, 31
	s_lshl_b64 s[0:1], s[18:19], 19
	s_add_u32 s4, s11, s0
	s_addc_u32 s5, s13, s1
	s_and_b64 s[0:1], s[20:21], exec
	s_cselect_b32 s5, s5, s27
	s_cselect_b32 s4, s4, s26
	s_ashr_i32 s17, s16, 31
	s_lshl_b64 s[0:1], s[16:17], 19
	s_add_u32 s15, s66, s0
	s_addc_u32 s17, s67, s1
	s_and_b64 s[0:1], s[20:21], exec
	s_cselect_b32 s17, s17, s29
	s_cselect_b32 s19, s15, s28
	s_ashr_i32 s15, s14, 31
	s_lshl_b64 s[0:1], s[14:15], 7
	s_add_u32 s4, s4, s0
	s_addc_u32 s5, s5, s1
	s_add_u32 s22, s19, s0
	s_addc_u32 s23, s17, s1
	s_and_b64 s[0:1], s[20:21], exec
	s_cselect_b32 s15, s23, s29
	s_cselect_b32 s17, s22, s28
	s_cselect_b32 s19, s5, s27
	s_cselect_b32 s36, s4, s26
	s_add_i32 s37, s33, -2
	s_add_u32 s26, s26, 0x40080
	s_addc_u32 s27, s27, 0
	s_add_u32 s38, s28, 0x100
	v_mov_b32_e32 v32, 0
	s_addc_u32 s39, s29, 0
	s_mov_b32 s28, 0
	v_mov_b32_e32 v33, v32
	v_mov_b32_e32 v34, v32
	v_mov_b32_e32 v35, v32
	v_mov_b32_e32 v36, v32
	v_mov_b32_e32 v37, v32
	v_mov_b32_e32 v38, v32
	v_mov_b32_e32 v39, v32
	v_mov_b32_e32 v48, v32
	v_mov_b32_e32 v49, v32
	v_mov_b32_e32 v50, v32
	v_mov_b32_e32 v51, v32
	v_mov_b32_e32 v52, v32
	v_mov_b32_e32 v53, v32
	v_mov_b32_e32 v54, v32
	v_mov_b32_e32 v55, v32
	v_mov_b32_e32 v64, v32
	v_mov_b32_e32 v65, v32
	v_mov_b32_e32 v66, v32
	v_mov_b32_e32 v67, v32
	v_mov_b32_e32 v68, v32
	v_mov_b32_e32 v69, v32
	v_mov_b32_e32 v70, v32
	v_mov_b32_e32 v71, v32
	v_mov_b32_e32 v80, v32
	v_mov_b32_e32 v81, v32
	v_mov_b32_e32 v82, v32
	v_mov_b32_e32 v83, v32
	v_mov_b32_e32 v84, v32
	v_mov_b32_e32 v85, v32
	v_mov_b32_e32 v86, v32
	v_mov_b32_e32 v87, v32
	v_mov_b32_e32 v40, v32
	v_mov_b32_e32 v41, v32
	v_mov_b32_e32 v42, v32
	v_mov_b32_e32 v43, v32
	v_mov_b32_e32 v44, v32
	v_mov_b32_e32 v45, v32
	v_mov_b32_e32 v46, v32
	v_mov_b32_e32 v47, v32
	v_mov_b32_e32 v56, v32
	v_mov_b32_e32 v57, v32
	v_mov_b32_e32 v58, v32
	v_mov_b32_e32 v59, v32
	v_mov_b32_e32 v60, v32
	v_mov_b32_e32 v61, v32
	v_mov_b32_e32 v62, v32
	v_mov_b32_e32 v63, v32
	v_mov_b32_e32 v72, v32
	v_mov_b32_e32 v73, v32
	v_mov_b32_e32 v74, v32
	v_mov_b32_e32 v75, v32
	v_mov_b32_e32 v76, v32
	v_mov_b32_e32 v77, v32
	v_mov_b32_e32 v78, v32
	v_mov_b32_e32 v79, v32
	v_mov_b32_e32 v88, v32
	v_mov_b32_e32 v89, v32
	v_mov_b32_e32 v90, v32
	v_mov_b32_e32 v91, v32
	v_mov_b32_e32 v92, v32
	v_mov_b32_e32 v93, v32
	v_mov_b32_e32 v94, v32
	v_mov_b32_e32 v95, v32
	v_mov_b32_e32 v96, v32
	v_mov_b32_e32 v97, v32
	v_mov_b32_e32 v98, v32
	v_mov_b32_e32 v99, v32
	v_mov_b32_e32 v100, v32
	v_mov_b32_e32 v101, v32
	v_mov_b32_e32 v102, v32
	v_mov_b32_e32 v103, v32
	v_mov_b32_e32 v112, v32
	v_mov_b32_e32 v113, v32
	v_mov_b32_e32 v114, v32
	v_mov_b32_e32 v115, v32
	v_mov_b32_e32 v116, v32
	v_mov_b32_e32 v117, v32
	v_mov_b32_e32 v118, v32
	v_mov_b32_e32 v119, v32
	v_mov_b32_e32 v128, v32
	v_mov_b32_e32 v129, v32
	v_mov_b32_e32 v130, v32
	v_mov_b32_e32 v131, v32
	v_mov_b32_e32 v132, v32
	v_mov_b32_e32 v133, v32
	v_mov_b32_e32 v134, v32
	v_mov_b32_e32 v135, v32
	v_mov_b32_e32 v144, v32
	v_mov_b32_e32 v145, v32
	v_mov_b32_e32 v146, v32
	v_mov_b32_e32 v147, v32
	v_mov_b32_e32 v148, v32
	v_mov_b32_e32 v149, v32
	v_mov_b32_e32 v150, v32
	v_mov_b32_e32 v151, v32
	v_mov_b32_e32 v104, v32
	v_mov_b32_e32 v105, v32
	v_mov_b32_e32 v106, v32
	v_mov_b32_e32 v107, v32
	v_mov_b32_e32 v108, v32
	v_mov_b32_e32 v109, v32
	v_mov_b32_e32 v110, v32
	v_mov_b32_e32 v111, v32
	v_mov_b32_e32 v120, v32
	v_mov_b32_e32 v121, v32
	v_mov_b32_e32 v122, v32
	v_mov_b32_e32 v123, v32
	v_mov_b32_e32 v124, v32
	v_mov_b32_e32 v125, v32
	v_mov_b32_e32 v126, v32
	v_mov_b32_e32 v127, v32
	v_mov_b32_e32 v136, v32
	v_mov_b32_e32 v137, v32
	v_mov_b32_e32 v138, v32
	v_mov_b32_e32 v139, v32
	v_mov_b32_e32 v140, v32
	v_mov_b32_e32 v141, v32
	v_mov_b32_e32 v142, v32
	v_mov_b32_e32 v143, v32
	v_mov_b32_e32 v152, v32
	v_mov_b32_e32 v153, v32
	v_mov_b32_e32 v154, v32
	v_mov_b32_e32 v155, v32
	v_mov_b32_e32 v156, v32
	v_mov_b32_e32 v157, v32
	v_mov_b32_e32 v158, v32
	v_mov_b32_e32 v159, v32
	.p2align	8

.LBB0_2315:
	s_ashr_i32 s17, s16, 31
	s_lshl_b64 s[0:1], s[16:17], 7
	s_and_b64 s[26:27], s[26:27], exec
	s_cselect_b32 s0, s0, 0
	s_cselect_b32 s1, s1, 0
	s_add_u32 s18, s18, s0
	s_addc_u32 s19, s19, s1
	s_add_u32 s20, s20, s0
	s_addc_u32 s21, s21, s1
	s_add_i32 s17, s30, -2
	s_add_u32 s31, s24, 0x100
	v_mov_b32_e32 v32, 0
	s_mov_b32 s28, 0
	s_addc_u32 s33, s25, 0
	v_mov_b32_e32 v33, v32
	v_mov_b32_e32 v34, v32
	v_mov_b32_e32 v35, v32
	v_mov_b32_e32 v36, v32
	v_mov_b32_e32 v37, v32
	v_mov_b32_e32 v38, v32
	v_mov_b32_e32 v39, v32
	v_mov_b32_e32 v48, v32
	v_mov_b32_e32 v49, v32
	v_mov_b32_e32 v50, v32
	v_mov_b32_e32 v51, v32
	v_mov_b32_e32 v52, v32
	v_mov_b32_e32 v53, v32
	v_mov_b32_e32 v54, v32
	v_mov_b32_e32 v55, v32
	v_mov_b32_e32 v64, v32
	v_mov_b32_e32 v65, v32
	v_mov_b32_e32 v66, v32
	v_mov_b32_e32 v67, v32
	v_mov_b32_e32 v68, v32
	v_mov_b32_e32 v69, v32
	v_mov_b32_e32 v70, v32
	v_mov_b32_e32 v71, v32
	v_mov_b32_e32 v80, v32
	v_mov_b32_e32 v81, v32
	v_mov_b32_e32 v82, v32
	v_mov_b32_e32 v83, v32
	v_mov_b32_e32 v84, v32
	v_mov_b32_e32 v85, v32
	v_mov_b32_e32 v86, v32
	v_mov_b32_e32 v87, v32
	v_mov_b32_e32 v40, v32
	v_mov_b32_e32 v41, v32
	v_mov_b32_e32 v42, v32
	v_mov_b32_e32 v43, v32
	v_mov_b32_e32 v44, v32
	v_mov_b32_e32 v45, v32
	v_mov_b32_e32 v46, v32
	v_mov_b32_e32 v47, v32
	v_mov_b32_e32 v56, v32
	v_mov_b32_e32 v57, v32
	v_mov_b32_e32 v58, v32
	v_mov_b32_e32 v59, v32
	v_mov_b32_e32 v60, v32
	v_mov_b32_e32 v61, v32
	v_mov_b32_e32 v62, v32
	v_mov_b32_e32 v63, v32
	v_mov_b32_e32 v72, v32
	v_mov_b32_e32 v73, v32
	v_mov_b32_e32 v74, v32
	v_mov_b32_e32 v75, v32
	v_mov_b32_e32 v76, v32
	v_mov_b32_e32 v77, v32
	v_mov_b32_e32 v78, v32
	v_mov_b32_e32 v79, v32
	v_mov_b32_e32 v88, v32
	v_mov_b32_e32 v89, v32
	v_mov_b32_e32 v90, v32
	v_mov_b32_e32 v91, v32
	v_mov_b32_e32 v92, v32
	v_mov_b32_e32 v93, v32
	v_mov_b32_e32 v94, v32
	v_mov_b32_e32 v95, v32
	v_mov_b32_e32 v96, v32
	v_mov_b32_e32 v97, v32
	v_mov_b32_e32 v98, v32
	v_mov_b32_e32 v99, v32
	v_mov_b32_e32 v100, v32
	v_mov_b32_e32 v101, v32
	v_mov_b32_e32 v102, v32
	v_mov_b32_e32 v103, v32
	v_mov_b32_e32 v112, v32
	v_mov_b32_e32 v113, v32
	v_mov_b32_e32 v114, v32
	v_mov_b32_e32 v115, v32
	v_mov_b32_e32 v116, v32
	v_mov_b32_e32 v117, v32
	v_mov_b32_e32 v118, v32
	v_mov_b32_e32 v119, v32
	v_mov_b32_e32 v128, v32
	v_mov_b32_e32 v129, v32
	v_mov_b32_e32 v130, v32
	v_mov_b32_e32 v131, v32
	v_mov_b32_e32 v132, v32
	v_mov_b32_e32 v133, v32
	v_mov_b32_e32 v134, v32
	v_mov_b32_e32 v135, v32
	v_mov_b32_e32 v144, v32
	v_mov_b32_e32 v145, v32
	v_mov_b32_e32 v146, v32
	v_mov_b32_e32 v147, v32
	v_mov_b32_e32 v148, v32
	v_mov_b32_e32 v149, v32
	v_mov_b32_e32 v150, v32
	v_mov_b32_e32 v151, v32
	v_mov_b32_e32 v104, v32
	v_mov_b32_e32 v105, v32
	v_mov_b32_e32 v106, v32
	v_mov_b32_e32 v107, v32
	v_mov_b32_e32 v108, v32
	v_mov_b32_e32 v109, v32
	v_mov_b32_e32 v110, v32
	v_mov_b32_e32 v111, v32
	v_mov_b32_e32 v120, v32
	v_mov_b32_e32 v121, v32
	v_mov_b32_e32 v122, v32
	v_mov_b32_e32 v123, v32
	v_mov_b32_e32 v124, v32
	v_mov_b32_e32 v125, v32
	v_mov_b32_e32 v126, v32
	v_mov_b32_e32 v127, v32
	v_mov_b32_e32 v136, v32
	v_mov_b32_e32 v137, v32
	v_mov_b32_e32 v138, v32
	v_mov_b32_e32 v139, v32
	v_mov_b32_e32 v140, v32
	v_mov_b32_e32 v141, v32
	v_mov_b32_e32 v142, v32
	v_mov_b32_e32 v143, v32
	v_mov_b32_e32 v152, v32
	v_mov_b32_e32 v153, v32
	v_mov_b32_e32 v154, v32
	v_mov_b32_e32 v155, v32
	v_mov_b32_e32 v156, v32
	v_mov_b32_e32 v157, v32
	v_mov_b32_e32 v158, v32
	v_mov_b32_e32 v159, v32
	.p2align	8
